# speedup vs baseline: 1.0092x; 1.0087x over previous
.LBB3_145:
	s_or_b64 exec, exec, s[54:55]
	v_div_scale_f32 v171, s[54:55], v163, v163, 1.0
	v_rcp_f32_e32 v197, v171
	v_div_scale_f32 v201, vcc, 1.0, v163, 1.0
	s_movk_i32 s69, 0x410
	v_fma_f32 v202, -v171, v197, 1.0
	v_fmac_f32_e32 v197, v202, v197
	v_mul_f32_e32 v202, v201, v197
	v_fma_f32 v203, -v171, v202, v201
	v_fmac_f32_e32 v202, v203, v197
	v_fma_f32 v171, -v171, v202, v201
	v_div_fmas_f32 v171, v171, v197, v202
	v_lshlrev_b32_e32 v197, 6, v189
	v_div_fixup_f32 v171, v171, v163, 1.0
	v_cmp_lt_f32_e32 vcc, 0, v163
	v_mul_lo_u32 v169, v169, s69
	v_and_b32_e32 v197, 0x3c0, v197
	v_cndmask_b32_e32 v163, 0, v171, vcc
	v_sub_u32_e32 v171, v160, v168
	v_add3_u32 v201, s99, v169, v197
	s_max_i32 s32, s33, s96
	s_max_i32 s32, s32, s97
	s_max_i32 s32, s32, s75
	s_cmp_gt_i32 s32, 32
	s_cbranch_scc1 .Lk4_slowst
	s_and_saveexec_b64 s[54:55], s[44:45]
	v_lshl_add_u32 v238, v171, 1, v201
	v_fma_mixlo_f16 v239, v163, v225, 0
	ds_write_b16 v238, v239
	v_fma_mixlo_f16 v240, v163, v224, 0
	ds_write_b16 v238, v240 offset:2
	v_fma_mixlo_f16 v241, v163, v223, 0
	ds_write_b16 v238, v241 offset:4
	v_fma_mixlo_f16 v242, v163, v222, 0
	ds_write_b16 v238, v242 offset:6
	v_fma_mixlo_f16 v239, v163, v221, 0
	ds_write_b16 v238, v239 offset:8
	v_fma_mixlo_f16 v240, v163, v220, 0
	ds_write_b16 v238, v240 offset:10
	v_fma_mixlo_f16 v241, v163, v219, 0
	ds_write_b16 v238, v241 offset:12
	v_fma_mixlo_f16 v242, v163, v218, 0
	ds_write_b16 v238, v242 offset:14
	s_cmp_eq_u64 s[34:35], 0
	s_cbranch_scc1 .Lk4_stdone
	v_fma_mixlo_f16 v239, v163, v217, 0
	ds_write_b16 v238, v239 offset:16
	v_fma_mixlo_f16 v240, v163, v216, 0
	ds_write_b16 v238, v240 offset:18
	v_fma_mixlo_f16 v241, v163, v215, 0
	ds_write_b16 v238, v241 offset:20
	v_fma_mixlo_f16 v242, v163, v214, 0
	ds_write_b16 v238, v242 offset:22
	s_cmp_eq_u64 s[24:25], 0
	s_cbranch_scc1 .Lk4_stdone
	v_fma_mixlo_f16 v239, v163, v200, 0
	ds_write_b16 v238, v239 offset:24
	v_fma_mixlo_f16 v240, v163, v199, 0
	ds_write_b16 v238, v240 offset:26
	v_fma_mixlo_f16 v241, v163, v198, 0
	ds_write_b16 v238, v241 offset:28
	v_fma_mixlo_f16 v242, v163, v196, 0
	ds_write_b16 v238, v242 offset:30
	s_cmp_eq_u64 s[16:17], 0
	s_cbranch_scc1 .Lk4_stdone
	v_fma_mixlo_f16 v239, v163, v195, 0
	ds_write_b16 v238, v239 offset:32
	v_fma_mixlo_f16 v240, v163, v176, 0
	ds_write_b16 v238, v240 offset:34
	v_fma_mixlo_f16 v241, v163, v175, 0
	ds_write_b16 v238, v241 offset:36
	v_fma_mixlo_f16 v242, v163, v174, 0
	ds_write_b16 v238, v242 offset:38
	s_cmp_eq_u64 s[8:9], 0
	s_cbranch_scc1 .Lk4_stdone
	v_fma_mixlo_f16 v239, v163, v173, 0
	ds_write_b16 v238, v239 offset:40
	v_fma_mixlo_f16 v240, v163, v172, 0
	ds_write_b16 v238, v240 offset:42
	v_fma_mixlo_f16 v241, v163, v164, 0
	ds_write_b16 v238, v241 offset:44
	v_fma_mixlo_f16 v242, v163, v161, 0
	ds_write_b16 v238, v242 offset:46
.Lk4_stdone:
	s_or_b64 exec, exec, s[54:55]
	s_and_saveexec_b64 s[4:5], s[0:1]
	s_cbranch_execz .LBB3_196
	s_branch .LBB3_194

	.amdhsa_kernel _Z8k_layer1PKiS0_PKfS2_PK15HIP_vector_typeIjLj4EEPKDv8_DF16_S9_S2_S2_S2_PDF16_PfSB_
		.amdhsa_group_segment_fixed_size 55232
		.amdhsa_private_segment_fixed_size 0
		.amdhsa_kernarg_size 360
		.amdhsa_user_sgpr_count 2
		.amdhsa_user_sgpr_dispatch_ptr 0
		.amdhsa_user_sgpr_queue_ptr 0
		.amdhsa_user_sgpr_kernarg_segment_ptr 1
		.amdhsa_user_sgpr_dispatch_id 0
		.amdhsa_user_sgpr_kernarg_preload_length 0
		.amdhsa_user_sgpr_kernarg_preload_offset 0
		.amdhsa_user_sgpr_private_segment_size 0
		.amdhsa_uses_dynamic_stack 0
		.amdhsa_enable_private_segment 0
		.amdhsa_system_sgpr_workgroup_id_x 1
		.amdhsa_system_sgpr_workgroup_id_y 0
		.amdhsa_system_sgpr_workgroup_id_z 0
		.amdhsa_system_sgpr_workgroup_info 0
		.amdhsa_system_vgpr_workitem_id 0
		.amdhsa_next_free_vgpr 243
		.amdhsa_next_free_sgpr 100
		.amdhsa_accum_offset 244
		.amdhsa_reserve_vcc 1
		.amdhsa_float_round_mode_32 0
		.amdhsa_float_round_mode_16_64 0
		.amdhsa_float_denorm_mode_32 3
		.amdhsa_float_denorm_mode_16_64 3
		.amdhsa_dx10_clamp 1
		.amdhsa_ieee_mode 1
		.amdhsa_fp16_overflow 0
		.amdhsa_tg_split 0
		.amdhsa_exception_fp_ieee_invalid_op 0
		.amdhsa_exception_fp_denorm_src 0
		.amdhsa_exception_fp_ieee_div_zero 0
		.amdhsa_exception_fp_ieee_overflow 0
		.amdhsa_exception_fp_ieee_underflow 0
		.amdhsa_exception_fp_ieee_inexact 0
		.amdhsa_exception_int_div_zero 0
	.end_amdhsa_kernel

amdhsa.kernels:
  - .agpr_count:     0
    .args:
      - .actual_access:  read_only
        .address_space:  global
        .offset:         0
        .size:           8
        .value_kind:     global_buffer
      - .actual_access:  read_only
        .address_space:  global
        .offset:         8
        .size:           8
        .value_kind:     global_buffer
      - .actual_access:  read_only
        .address_space:  global
        .offset:         16
        .size:           8
        .value_kind:     global_buffer
      - .actual_access:  read_only
        .address_space:  global
        .offset:         24
        .size:           8
        .value_kind:     global_buffer
      - .actual_access:  read_only
        .address_space:  global
        .offset:         32
        .size:           8
        .value_kind:     global_buffer
      - .actual_access:  write_only
        .address_space:  global
        .offset:         40
        .size:           8
        .value_kind:     global_buffer
      - .actual_access:  write_only
        .address_space:  global
        .offset:         48
        .size:           8
        .value_kind:     global_buffer
      - .actual_access:  write_only
        .address_space:  global
        .offset:         56
        .size:           8
        .value_kind:     global_buffer
      - .actual_access:  write_only
        .address_space:  global
        .offset:         64
        .size:           8
        .value_kind:     global_buffer
    .group_segment_fixed_size: 1024
    .kernarg_segment_align: 8
    .kernarg_segment_size: 72
    .language:       OpenCL C
    .language_version:
      - 2
      - 0
    .max_flat_workgroup_size: 512
    .name:           _Z11k_hist_prepPKiPKfS2_S2_S2_PiPfPDF16_S5_
    .private_segment_fixed_size: 0
    .sgpr_count:     20
    .sgpr_spill_count: 0
    .symbol:         _Z11k_hist_prepPKiPKfS2_S2_S2_PiPfPDF16_S5_.kd
    .uniform_work_group_size: 1
    .uses_dynamic_stack: false
    .vgpr_count:     42
    .vgpr_spill_count: 0
    .wavefront_size: 64
  - .agpr_count:     0
    .args:
      - .actual_access:  read_only
        .address_space:  global
        .offset:         0
        .size:           8
        .value_kind:     global_buffer
      - .actual_access:  read_only
        .address_space:  global
        .offset:         8
        .size:           8
        .value_kind:     global_buffer
      - .actual_access:  write_only
        .address_space:  global
        .offset:         16
        .size:           8
        .value_kind:     global_buffer
      - .actual_access:  write_only
        .address_space:  global
        .offset:         24
        .size:           8
        .value_kind:     global_buffer
      - .actual_access:  read_only
        .address_space:  global
        .offset:         32
        .size:           8
        .value_kind:     global_buffer
      - .actual_access:  read_only
        .address_space:  global
        .offset:         40
        .size:           8
        .value_kind:     global_buffer
      - .actual_access:  write_only
        .address_space:  global
        .offset:         48
        .size:           8
        .value_kind:     global_buffer
      - .actual_access:  write_only
        .address_space:  global
        .offset:         56
        .size:           8
        .value_kind:     global_buffer
      - .actual_access:  write_only
        .address_space:  global
        .offset:         64
        .size:           8
        .value_kind:     global_buffer
    .group_segment_fixed_size: 9344
    .kernarg_segment_align: 8
    .kernarg_segment_size: 72
    .language:       OpenCL C
    .language_version:
      - 2
      - 0
    .max_flat_workgroup_size: 512
    .name:           _Z14k_scatter_nodePKiS0_PjPiPKfS4_PfS5_PDF16_
    .private_segment_fixed_size: 0
    .sgpr_count:     106
    .sgpr_spill_count: 10
    .symbol:         _Z14k_scatter_nodePKiS0_PjPiPKfS4_PfS5_PDF16_.kd
    .uniform_work_group_size: 1
    .uses_dynamic_stack: false
    .vgpr_count:     118
    .vgpr_spill_count: 0
    .wavefront_size: 64
  - .agpr_count:     0
    .args:
      - .actual_access:  read_only
        .address_space:  global
        .offset:         0
        .size:           8
        .value_kind:     global_buffer
      - .actual_access:  read_only
        .address_space:  global
        .offset:         8
        .size:           8
        .value_kind:     global_buffer
      - .actual_access:  write_only
        .address_space:  global
        .offset:         16
        .size:           8
        .value_kind:     global_buffer
      - .actual_access:  write_only
        .address_space:  global
        .offset:         24
        .size:           8
        .value_kind:     global_buffer
    .group_segment_fixed_size: 3072
    .kernarg_segment_align: 8
    .kernarg_segment_size: 32
    .language:       OpenCL C
    .language_version:
      - 2
      - 0
    .max_flat_workgroup_size: 1024
    .name:           _Z5k_csrPKjPKiPiS3_
    .private_segment_fixed_size: 0
    .sgpr_count:     34
    .sgpr_spill_count: 0
    .symbol:         _Z5k_csrPKjPKiPiS3_.kd
    .uniform_work_group_size: 1
    .uses_dynamic_stack: false
    .vgpr_count:     18
    .vgpr_spill_count: 0
    .wavefront_size: 64
  - .agpr_count:     0
    .args:
      - .actual_access:  read_only
        .address_space:  global
        .offset:         0
        .size:           8
        .value_kind:     global_buffer
      - .actual_access:  read_only
        .address_space:  global
        .offset:         8
        .size:           8
        .value_kind:     global_buffer
      - .actual_access:  read_only
        .address_space:  global
        .offset:         16
        .size:           8
        .value_kind:     global_buffer
      - .actual_access:  read_only
        .address_space:  global
        .offset:         24
        .size:           8
        .value_kind:     global_buffer
      - .actual_access:  read_only
        .address_space:  global
        .offset:         32
        .size:           8
        .value_kind:     global_buffer
      - .actual_access:  read_only
        .address_space:  global
        .offset:         40
        .size:           8
        .value_kind:     global_buffer
      - .actual_access:  read_only
        .address_space:  global
        .offset:         48
        .size:           8
        .value_kind:     global_buffer
      - .actual_access:  read_only
        .address_space:  global
        .offset:         56
        .size:           8
        .value_kind:     global_buffer
      - .actual_access:  read_only
        .address_space:  global
        .offset:         64
        .size:           8
        .value_kind:     global_buffer
      - .actual_access:  read_only
        .address_space:  global
        .offset:         72
        .size:           8
        .value_kind:     global_buffer
      - .actual_access:  write_only
        .address_space:  global
        .offset:         80
        .size:           8
        .value_kind:     global_buffer
      - .actual_access:  write_only
        .address_space:  global
        .offset:         88
        .size:           8
        .value_kind:     global_buffer
      - .actual_access:  write_only
        .address_space:  global
        .offset:         96
        .size:           8
        .value_kind:     global_buffer
      - .offset:         104
        .size:           4
        .value_kind:     hidden_block_count_x
      - .offset:         108
        .size:           4
        .value_kind:     hidden_block_count_y
      - .offset:         112
        .size:           4
        .value_kind:     hidden_block_count_z
      - .offset:         116
        .size:           2
        .value_kind:     hidden_group_size_x
      - .offset:         118
        .size:           2
        .value_kind:     hidden_group_size_y
      - .offset:         120
        .size:           2
        .value_kind:     hidden_group_size_z
      - .offset:         122
        .size:           2
        .value_kind:     hidden_remainder_x
      - .offset:         124
        .size:           2
        .value_kind:     hidden_remainder_y
      - .offset:         126
        .size:           2
        .value_kind:     hidden_remainder_z
      - .offset:         144
        .size:           8
        .value_kind:     hidden_global_offset_x
      - .offset:         152
        .size:           8
        .value_kind:     hidden_global_offset_y
      - .offset:         160
        .size:           8
        .value_kind:     hidden_global_offset_z
      - .offset:         168
        .size:           2
        .value_kind:     hidden_grid_dims
    .group_segment_fixed_size: 55232
    .kernarg_segment_align: 8
    .kernarg_segment_size: 360
    .language:       OpenCL C
    .language_version:
      - 2
      - 0
    .max_flat_workgroup_size: 256
    .name:           _Z8k_layer1PKiS0_PKfS2_PK15HIP_vector_typeIjLj4EEPKDv8_DF16_S9_S2_S2_S2_PDF16_PfSB_
    .private_segment_fixed_size: 0
    .sgpr_count:     106
    .sgpr_spill_count: 7
    .symbol:         _Z8k_layer1PKiS0_PKfS2_PK15HIP_vector_typeIjLj4EEPKDv8_DF16_S9_S2_S2_S2_PDF16_PfSB_.kd
    .uniform_work_group_size: 1
    .uses_dynamic_stack: false
    .vgpr_count:     243
    .vgpr_spill_count: 0
    .wavefront_size: 64
  - .agpr_count:     0
    .args:
      - .actual_access:  read_only
        .address_space:  global
        .offset:         0
        .size:           8
        .value_kind:     global_buffer
      - .actual_access:  read_only
        .address_space:  global
        .offset:         8
        .size:           8
        .value_kind:     global_buffer
      - .actual_access:  read_only
        .address_space:  global
        .offset:         16
        .size:           8
        .value_kind:     global_buffer
      - .actual_access:  read_only
        .address_space:  global
        .offset:         24
        .size:           8
        .value_kind:     global_buffer
      - .actual_access:  read_only
        .address_space:  global
        .offset:         32
        .size:           8
        .value_kind:     global_buffer
      - .actual_access:  read_only
        .address_space:  global
        .offset:         40
        .size:           8
        .value_kind:     global_buffer
      - .actual_access:  write_only
        .address_space:  global
        .offset:         48
        .size:           8
        .value_kind:     global_buffer
    .group_segment_fixed_size: 0
    .kernarg_segment_align: 8
    .kernarg_segment_size: 56
    .language:       OpenCL C
    .language_version:
      - 2
      - 0
    .max_flat_workgroup_size: 256
    .name:           _Z8k_layer2PKiS0_PKfS2_PK15HIP_vector_typeIjLj4EES2_Pf
    .private_segment_fixed_size: 0
    .sgpr_count:     52
    .sgpr_spill_count: 0
    .symbol:         _Z8k_layer2PKiS0_PKfS2_PK15HIP_vector_typeIjLj4EES2_Pf.kd
    .uniform_work_group_size: 1
    .uses_dynamic_stack: false
    .vgpr_count:     70
    .vgpr_spill_count: 0
    .wavefront_size: 64
